# up-front convert phase skips layer-1 w_in only on the 256-workgroup grid (guard); otherwise as previous version
# speedup vs baseline: 1.0107x; 1.0044x over previous
.LBB0_990:
	s_mul_hi_u32 s6, s30, s26
	s_mul_i32 s6, s6, s33
	s_sub_i32 s6, s30, s6
	s_sub_i32 s7, s6, s33
	s_cmp_ge_u32 s6, s33
	s_cselect_b32 s6, s7, s6
	s_sub_i32 s7, s6, s33
	s_cmp_ge_u32 s6, s33
	s_cselect_b32 s6, s7, s6
	s_sub_i32 s6, s19, s6
	s_mul_hi_u32 s7, s6, s26
	s_mul_i32 s7, s7, s33
	s_sub_i32 s6, s6, s7
	s_sub_i32 s7, s6, s33
	s_cmp_ge_u32 s6, s33
	s_cselect_b32 s6, s7, s6
	s_sub_i32 s7, s6, s33
	s_cmp_ge_u32 s6, s33
	s_cselect_b32 s6, s7, s6
	s_cmpk_lg_i32 s52, 0x100
	s_cbranch_scc1 .Lcvt_do_win
	s_cmp_eq_u32 s16, 1
	s_cbranch_scc1 .LBB0_993
.Lcvt_do_win:
	s_cmpk_gt_i32 s6, 0x2eff
	s_cbranch_scc1 .LBB0_993
	s_mul_i32 s7, s16, 0x2f00000
	s_add_u32 s7, s3, s7
	s_mul_i32 s10, s16, 0x5e00000
	s_mov_b32 s11, s17
	s_addc_u32 s8, s18, 0
	v_lshl_add_u64 v[24:25], v[6:7], 0, s[10:11]
	s_lshl_b32 s9, s6, 5
